# gemm8 epilogue: per-group uniform bf16/f16 branch diamonds replaced by two straight-line pack copies
# speedup vs baseline: 1.0107x; 1.0054x over previous
.LBB15_14:
	s_and_b64 vcc, exec, s[0:1]
	s_cbranch_vccz .Lg8_pack_bf16
	s_and_b64 vcc, exec, s[0:1]
	v_cvt_pk_f16_f32 v130, v126, v127
	v_cvt_pk_f16_f32 v131, v128, v129
	v_lshrrev_b32_e32 v132, 4, v0
	v_lshlrev_b32_e32 v126, 3, v132
	v_lshlrev_b32_e32 v133, 3, v145
	v_lshrrev_b32_e32 v134, 1, v135
	v_and_b32_e32 v126, 8, v126
	v_add_u32_e32 v128, 0, v126
	v_or_b32_e32 v126, v136, v144
	v_bitop3_b32 v127, v133, v144, v134 bitop3:0x36
	v_lshl_add_u32 v132, v127, 4, v128
	v_lshlrev_b32_e32 v129, 9, v126
	v_cndmask_b32_e64 v126, 0, 1, s[0:1]
	v_add_u32_e32 v135, v132, v129
	v_cmp_ne_u32_e64 s[2:3], 1, v126
	s_andn2_b64 vcc, exec, s[0:1]
	s_waitcnt vmcnt(0)
	ds_write_b64 v135, v[130:131]
	v_cvt_pk_f16_f32 v126, v122, v123
	v_cvt_pk_f16_f32 v127, v124, v125
	s_and_b64 vcc, exec, s[2:3]
	ds_write_b64 v135, v[126:127] offset:8192
	v_cvt_pk_f16_f32 v122, v118, v119
	v_cvt_pk_f16_f32 v123, v120, v121
	v_or_b32_e32 v124, v133, v134
	v_bitop3_b32 v118, v124, v144, 2 bitop3:0x36
	v_lshl_add_u32 v120, v118, 4, v128
	v_add_u32_e32 v121, v120, v129
	s_and_b64 vcc, exec, s[2:3]
	ds_write_b64 v121, v[122:123]
	v_cvt_pk_f16_f32 v118, v114, v115
	v_cvt_pk_f16_f32 v119, v116, v117
	s_and_b64 vcc, exec, s[2:3]
	ds_write_b64 v121, v[118:119] offset:8192
	v_cvt_pk_f16_f32 v114, v110, v111
	v_cvt_pk_f16_f32 v115, v112, v113
	v_bitop3_b32 v110, v124, v144, 4 bitop3:0x36
	v_lshl_add_u32 v112, v110, 4, v128
	v_add_u32_e32 v113, v112, v129
	s_and_b64 vcc, exec, s[2:3]
	ds_write_b64 v113, v[114:115]
	v_cvt_pk_f16_f32 v110, v106, v107
	v_cvt_pk_f16_f32 v111, v108, v109
	s_and_b64 vcc, exec, s[2:3]
	ds_write_b64 v113, v[110:111] offset:8192
	v_cvt_pk_f16_f32 v106, v102, v103
	v_cvt_pk_f16_f32 v107, v104, v105
	v_bitop3_b32 v102, v124, v144, 6 bitop3:0x36
	v_lshl_add_u32 v104, v102, 4, v128
	v_add_u32_e32 v105, v104, v129
	s_and_b64 vcc, exec, s[2:3]
	ds_write_b64 v105, v[106:107]
	v_cvt_pk_f16_f32 v102, v98, v99
	v_cvt_pk_f16_f32 v103, v100, v101
	s_and_b64 vcc, exec, s[2:3]
	ds_write_b64 v105, v[102:103] offset:8192
	v_cvt_pk_f16_f32 v98, v94, v95
	v_cvt_pk_f16_f32 v99, v96, v97
	v_or_b32_e32 v96, 0x10000, v129
	v_add_u32_e32 v97, v132, v96
	s_and_b64 vcc, exec, s[2:3]
	ds_write_b64 v97, v[98:99]
	v_cvt_pk_f16_f32 v94, v90, v91
	v_cvt_pk_f16_f32 v95, v92, v93
	s_and_b64 vcc, exec, s[2:3]
	ds_write_b64 v97, v[94:95] offset:8192
	v_cvt_pk_f16_f32 v90, v86, v87
	v_cvt_pk_f16_f32 v91, v88, v89
	v_add_u32_e32 v88, v120, v96
	s_and_b64 vcc, exec, s[2:3]
	ds_write_b64 v88, v[90:91]
	v_cvt_pk_f16_f32 v86, v82, v83
	v_cvt_pk_f16_f32 v87, v84, v85
	s_and_b64 vcc, exec, s[2:3]
	ds_write_b64 v88, v[86:87] offset:8192
	v_cvt_pk_f16_f32 v82, v78, v79
	v_cvt_pk_f16_f32 v83, v80, v81
	v_add_u32_e32 v80, v112, v96
	s_and_b64 vcc, exec, s[2:3]
	ds_write_b64 v80, v[82:83]
	v_cvt_pk_f16_f32 v78, v74, v75
	v_cvt_pk_f16_f32 v79, v76, v77
	s_and_b64 vcc, exec, s[2:3]
	ds_write_b64 v80, v[78:79] offset:8192
	v_cvt_pk_f16_f32 v74, v70, v71
	v_cvt_pk_f16_f32 v75, v72, v73
	v_add_u32_e32 v72, v104, v96
	s_and_b64 vcc, exec, s[2:3]
	ds_write_b64 v72, v[74:75]
	v_cvt_pk_f16_f32 v70, v66, v67
	v_cvt_pk_f16_f32 v71, v68, v69
	s_and_b64 vcc, exec, s[2:3]
	ds_write_b64 v72, v[70:71] offset:8192
	v_cvt_pk_f16_f32 v66, v62, v63
	v_cvt_pk_f16_f32 v67, v64, v65
	v_bitop3_b32 v62, v124, v144, 16 bitop3:0x36
	v_lshl_add_u32 v64, v62, 4, v128
	v_add_u32_e32 v65, v64, v129
	s_and_b64 vcc, exec, s[2:3]
	ds_write_b64 v65, v[66:67]
	v_cvt_pk_f16_f32 v62, v58, v59
	v_cvt_pk_f16_f32 v63, v60, v61
	s_and_b64 vcc, exec, s[2:3]
	ds_write_b64 v65, v[62:63] offset:8192
	v_cvt_pk_f16_f32 v58, v54, v55
	v_cvt_pk_f16_f32 v59, v56, v57
	v_add_u32_e32 v54, 18, v124
	v_xor_b32_e32 v54, v54, v144
	v_lshl_add_u32 v56, v54, 4, v128
	v_add_u32_e32 v57, v56, v129
	s_and_b64 vcc, exec, s[2:3]
	ds_write_b64 v57, v[58:59]
	v_cvt_pk_f16_f32 v54, v50, v51
	v_cvt_pk_f16_f32 v55, v52, v53
	s_and_b64 vcc, exec, s[2:3]
	ds_write_b64 v57, v[54:55] offset:8192
	v_cvt_pk_f16_f32 v50, v46, v47
	v_cvt_pk_f16_f32 v51, v48, v49
	v_add_u32_e32 v46, 20, v124
	v_xor_b32_e32 v46, v46, v144
	v_lshl_add_u32 v48, v46, 4, v128
	v_add_u32_e32 v49, v48, v129
	s_and_b64 vcc, exec, s[2:3]
	ds_write_b64 v49, v[50:51]
	v_cvt_pk_f16_f32 v46, v42, v43
	v_cvt_pk_f16_f32 v47, v44, v45
	s_and_b64 vcc, exec, s[2:3]
	ds_write_b64 v49, v[46:47] offset:8192
	v_cvt_pk_f16_f32 v42, v38, v39
	v_cvt_pk_f16_f32 v43, v40, v41
	v_add_u32_e32 v38, 22, v124
	v_xor_b32_e32 v38, v38, v144
	v_lshl_add_u32 v40, v38, 4, v128
	v_add_u32_e32 v41, v40, v129
	s_and_b64 vcc, exec, s[2:3]
	ds_write_b64 v41, v[42:43]
	v_cvt_pk_f16_f32 v38, v34, v35
	v_cvt_pk_f16_f32 v39, v36, v37
	s_and_b64 vcc, exec, s[2:3]
	ds_write_b64 v41, v[38:39] offset:8192
	v_cvt_pk_f16_f32 v34, v30, v31
	v_cvt_pk_f16_f32 v35, v32, v33
	v_add_u32_e32 v32, v64, v96
	s_and_b64 vcc, exec, s[2:3]
	ds_write_b64 v32, v[34:35]
	v_cvt_pk_f16_f32 v30, v26, v27
	v_cvt_pk_f16_f32 v31, v28, v29
	s_and_b64 vcc, exec, s[2:3]
	ds_write_b64 v32, v[30:31] offset:8192
	v_cvt_pk_f16_f32 v26, v22, v23
	v_cvt_pk_f16_f32 v27, v24, v25
	v_add_u32_e32 v24, v56, v96
	s_and_b64 vcc, exec, s[2:3]
	ds_write_b64 v24, v[26:27]
	v_cvt_pk_f16_f32 v22, v18, v19
	v_cvt_pk_f16_f32 v23, v20, v21
	s_and_b64 vcc, exec, s[2:3]
	ds_write_b64 v24, v[22:23] offset:8192
	v_cvt_pk_f16_f32 v18, v14, v15
	v_cvt_pk_f16_f32 v19, v16, v17
	v_add_u32_e32 v16, v48, v96
	s_and_b64 vcc, exec, s[2:3]
	ds_write_b64 v16, v[18:19]
	v_cvt_pk_f16_f32 v14, v10, v11
	v_cvt_pk_f16_f32 v15, v12, v13
	s_and_b64 vcc, exec, s[2:3]
	ds_write_b64 v16, v[14:15] offset:8192
	v_cvt_pk_f16_f32 v10, v6, v7
	v_cvt_pk_f16_f32 v11, v8, v9
	v_add_u32_e32 v8, v40, v96
	s_and_b64 vcc, exec, s[2:3]
	ds_write_b64 v8, v[10:11]
	v_cvt_pk_f16_f32 v6, v2, v3
	v_cvt_pk_f16_f32 v7, v4, v5
	s_branch .LBB15_142
.Lg8_pack_bf16:
	s_and_b64 vcc, exec, s[0:1]
	v_lshrrev_b32_e32 v132, 4, v0
	v_cvt_pk_bf16_f32 v130, v126, v127
	v_cvt_pk_bf16_f32 v131, v128, v129
	v_lshlrev_b32_e32 v126, 3, v132
	v_lshlrev_b32_e32 v133, 3, v145
	v_lshrrev_b32_e32 v134, 1, v135
	v_and_b32_e32 v126, 8, v126
	v_add_u32_e32 v128, 0, v126
	v_or_b32_e32 v126, v136, v144
	v_bitop3_b32 v127, v133, v144, v134 bitop3:0x36
	v_lshl_add_u32 v132, v127, 4, v128
	v_lshlrev_b32_e32 v129, 9, v126
	v_cndmask_b32_e64 v126, 0, 1, s[0:1]
	v_add_u32_e32 v135, v132, v129
	v_cmp_ne_u32_e64 s[2:3], 1, v126
	s_andn2_b64 vcc, exec, s[0:1]
	s_waitcnt vmcnt(0)
	ds_write_b64 v135, v[130:131]
	v_cvt_pk_bf16_f32 v126, v122, v123
	v_cvt_pk_bf16_f32 v127, v124, v125
	s_and_b64 vcc, exec, s[2:3]
	ds_write_b64 v135, v[126:127] offset:8192
	v_or_b32_e32 v124, v133, v134
	v_cvt_pk_bf16_f32 v122, v118, v119
	v_cvt_pk_bf16_f32 v123, v120, v121
	v_bitop3_b32 v118, v124, v144, 2 bitop3:0x36
	v_lshl_add_u32 v120, v118, 4, v128
	v_add_u32_e32 v121, v120, v129
	s_and_b64 vcc, exec, s[2:3]
	ds_write_b64 v121, v[122:123]
	v_cvt_pk_bf16_f32 v118, v114, v115
	v_cvt_pk_bf16_f32 v119, v116, v117
	s_and_b64 vcc, exec, s[2:3]
	ds_write_b64 v121, v[118:119] offset:8192
	v_cvt_pk_bf16_f32 v114, v110, v111
	v_cvt_pk_bf16_f32 v115, v112, v113
	v_bitop3_b32 v110, v124, v144, 4 bitop3:0x36
	v_lshl_add_u32 v112, v110, 4, v128
	v_add_u32_e32 v113, v112, v129
	s_and_b64 vcc, exec, s[2:3]
	ds_write_b64 v113, v[114:115]
	v_cvt_pk_bf16_f32 v110, v106, v107
	v_cvt_pk_bf16_f32 v111, v108, v109
	s_and_b64 vcc, exec, s[2:3]
	ds_write_b64 v113, v[110:111] offset:8192
	v_cvt_pk_bf16_f32 v106, v102, v103
	v_cvt_pk_bf16_f32 v107, v104, v105
	v_bitop3_b32 v102, v124, v144, 6 bitop3:0x36
	v_lshl_add_u32 v104, v102, 4, v128
	v_add_u32_e32 v105, v104, v129
	s_and_b64 vcc, exec, s[2:3]
	ds_write_b64 v105, v[106:107]
	v_cvt_pk_bf16_f32 v102, v98, v99
	v_cvt_pk_bf16_f32 v103, v100, v101
	s_and_b64 vcc, exec, s[2:3]
	ds_write_b64 v105, v[102:103] offset:8192
	v_cvt_pk_bf16_f32 v98, v94, v95
	v_cvt_pk_bf16_f32 v99, v96, v97
	v_or_b32_e32 v96, 0x10000, v129
	v_add_u32_e32 v97, v132, v96
	s_and_b64 vcc, exec, s[2:3]
	ds_write_b64 v97, v[98:99]
	v_cvt_pk_bf16_f32 v94, v90, v91
	v_cvt_pk_bf16_f32 v95, v92, v93
	s_and_b64 vcc, exec, s[2:3]
	ds_write_b64 v97, v[94:95] offset:8192
	v_cvt_pk_bf16_f32 v90, v86, v87
	v_cvt_pk_bf16_f32 v91, v88, v89
	v_add_u32_e32 v88, v120, v96
	s_and_b64 vcc, exec, s[2:3]
	ds_write_b64 v88, v[90:91]
	v_cvt_pk_bf16_f32 v86, v82, v83
	v_cvt_pk_bf16_f32 v87, v84, v85
	s_and_b64 vcc, exec, s[2:3]
	ds_write_b64 v88, v[86:87] offset:8192
	v_cvt_pk_bf16_f32 v82, v78, v79
	v_cvt_pk_bf16_f32 v83, v80, v81
	v_add_u32_e32 v80, v112, v96
	s_and_b64 vcc, exec, s[2:3]
	ds_write_b64 v80, v[82:83]
	v_cvt_pk_bf16_f32 v78, v74, v75
	v_cvt_pk_bf16_f32 v79, v76, v77
	s_and_b64 vcc, exec, s[2:3]
	ds_write_b64 v80, v[78:79] offset:8192
	v_cvt_pk_bf16_f32 v74, v70, v71
	v_cvt_pk_bf16_f32 v75, v72, v73
	v_add_u32_e32 v72, v104, v96
	s_and_b64 vcc, exec, s[2:3]
	ds_write_b64 v72, v[74:75]
	v_cvt_pk_bf16_f32 v70, v66, v67
	v_cvt_pk_bf16_f32 v71, v68, v69
	s_and_b64 vcc, exec, s[2:3]
	ds_write_b64 v72, v[70:71] offset:8192
	v_cvt_pk_bf16_f32 v66, v62, v63
	v_cvt_pk_bf16_f32 v67, v64, v65
	v_bitop3_b32 v62, v124, v144, 16 bitop3:0x36
	v_lshl_add_u32 v64, v62, 4, v128
	v_add_u32_e32 v65, v64, v129
	s_and_b64 vcc, exec, s[2:3]
	ds_write_b64 v65, v[66:67]
	v_cvt_pk_bf16_f32 v62, v58, v59
	v_cvt_pk_bf16_f32 v63, v60, v61
	s_and_b64 vcc, exec, s[2:3]
	ds_write_b64 v65, v[62:63] offset:8192
	v_cvt_pk_bf16_f32 v58, v54, v55
	v_cvt_pk_bf16_f32 v59, v56, v57
	v_add_u32_e32 v54, 18, v124
	v_xor_b32_e32 v54, v54, v144
	v_lshl_add_u32 v56, v54, 4, v128
	v_add_u32_e32 v57, v56, v129
	s_and_b64 vcc, exec, s[2:3]
	ds_write_b64 v57, v[58:59]
	v_cvt_pk_bf16_f32 v54, v50, v51
	v_cvt_pk_bf16_f32 v55, v52, v53
	s_and_b64 vcc, exec, s[2:3]
	ds_write_b64 v57, v[54:55] offset:8192
	v_cvt_pk_bf16_f32 v50, v46, v47
	v_cvt_pk_bf16_f32 v51, v48, v49
	v_add_u32_e32 v46, 20, v124
	v_xor_b32_e32 v46, v46, v144
	v_lshl_add_u32 v48, v46, 4, v128
	v_add_u32_e32 v49, v48, v129
	s_and_b64 vcc, exec, s[2:3]
	ds_write_b64 v49, v[50:51]
	v_cvt_pk_bf16_f32 v46, v42, v43
	v_cvt_pk_bf16_f32 v47, v44, v45
	s_and_b64 vcc, exec, s[2:3]
	ds_write_b64 v49, v[46:47] offset:8192
	v_cvt_pk_bf16_f32 v42, v38, v39
	v_cvt_pk_bf16_f32 v43, v40, v41
	v_add_u32_e32 v38, 22, v124
	v_xor_b32_e32 v38, v38, v144
	v_lshl_add_u32 v40, v38, 4, v128
	v_add_u32_e32 v41, v40, v129
	s_and_b64 vcc, exec, s[2:3]
	ds_write_b64 v41, v[42:43]
	v_cvt_pk_bf16_f32 v38, v34, v35
	v_cvt_pk_bf16_f32 v39, v36, v37
	s_and_b64 vcc, exec, s[2:3]
	ds_write_b64 v41, v[38:39] offset:8192
	v_cvt_pk_bf16_f32 v34, v30, v31
	v_cvt_pk_bf16_f32 v35, v32, v33
	v_add_u32_e32 v32, v64, v96
	s_and_b64 vcc, exec, s[2:3]
	ds_write_b64 v32, v[34:35]
	v_cvt_pk_bf16_f32 v30, v26, v27
	v_cvt_pk_bf16_f32 v31, v28, v29
	s_and_b64 vcc, exec, s[2:3]
	ds_write_b64 v32, v[30:31] offset:8192
	v_cvt_pk_bf16_f32 v26, v22, v23
	v_cvt_pk_bf16_f32 v27, v24, v25
	v_add_u32_e32 v24, v56, v96
	s_and_b64 vcc, exec, s[2:3]
	ds_write_b64 v24, v[26:27]
	v_cvt_pk_bf16_f32 v22, v18, v19
	v_cvt_pk_bf16_f32 v23, v20, v21
	s_and_b64 vcc, exec, s[2:3]
	ds_write_b64 v24, v[22:23] offset:8192
	v_cvt_pk_bf16_f32 v18, v14, v15
	v_cvt_pk_bf16_f32 v19, v16, v17
	v_add_u32_e32 v16, v48, v96
	s_and_b64 vcc, exec, s[2:3]
	ds_write_b64 v16, v[18:19]
	v_cvt_pk_bf16_f32 v14, v10, v11
	v_cvt_pk_bf16_f32 v15, v12, v13
	s_and_b64 vcc, exec, s[2:3]
	ds_write_b64 v16, v[14:15] offset:8192
	v_cvt_pk_bf16_f32 v10, v6, v7
	v_cvt_pk_bf16_f32 v11, v8, v9
	v_add_u32_e32 v8, v40, v96
	s_and_b64 vcc, exec, s[2:3]
	ds_write_b64 v8, v[10:11]
	v_cvt_pk_bf16_f32 v6, v2, v3
	v_cvt_pk_bf16_f32 v7, v4, v5
